# speedup vs baseline: 1.0085x; 1.0053x over previous
.LBB2_4:
	s_and_b32 s0, s23, 0x3fffffc0
	s_lshl_b32 s0, s0, 2
	s_lshl_b64 s[10:11], s[2:3], 9
	s_add_i32 s23, s0, 0
	s_add_u32 s0, s14, 0x6000
	s_waitcnt vmcnt(0) lgkmcnt(0)
	s_barrier
	s_addc_u32 s1, s15, 0
	s_mov_b32 s2, m0
	s_mov_b32 m0, s24
	s_nop 0
	global_load_lds_dwordx4 v189, s[0:1]
	s_mov_b32 m0, s2
	s_add_u32 s0, s12, 0x2000
	s_addc_u32 s1, s13, 0
	s_cmp_lg_u32 0, -1
	s_cselect_b32 s2, 0, 0
	s_add_i32 s2, s2, s22
	s_add_i32 s2, s2, 0x8000
	s_mov_b32 s4, m0
	s_mov_b32 m0, s2
	s_nop 0
	global_load_lds_dwordx4 v189, s[0:1]
	s_mov_b32 m0, s4
	ds_read_b128 v[172:175], v190 offset:8192
	ds_read_b128 v[168:171], v190 offset:8704
	ds_read_b128 v[164:167], v190 offset:10240
	ds_read_b128 v[160:163], v190 offset:10752
	ds_read_b128 v[156:159], v190 offset:12288
	ds_read_b128 v[152:155], v190 offset:12800
	ds_read_b128 v[148:151], v190 offset:14336
	ds_read_b128 v[144:147], v190 offset:14848
	s_mov_b32 s3, 0
	s_add_i32 s2, s28, s27
	s_lshl_b64 s[4:5], s[2:3], 18
	v_lshlrev_b32_e32 v2, 1, v1
	v_lshlrev_b32_e32 v3, 3, v0
	s_add_u32 s2, s8, s4
	v_and_b32_e32 v2, 32, v2
	v_and_b32_e32 v3, 24, v3
	v_lshlrev_b32_e32 v185, 4, v0
	s_waitcnt vmcnt(2) lgkmcnt(0)
	s_barrier
	s_addc_u32 s4, s9, s5
	v_add3_u32 v2, 0, v2, v3
	v_lshlrev_b32_e32 v3, 8, v18
	v_and_b32_e32 v0, 0xc0, v185
	s_add_u32 s27, s2, 0x2000
	v_mov_b32_e32 v188, 0
	v_lshrrev_b32_e32 v183, 4, v1
	v_add3_u32 v187, v2, v3, v0
	s_mov_b32 s26, -1
	v_cmp_gt_u32_e64 s[0:1], 32, v1
	v_lshl_add_u32 v186, v181, 2, s23
	s_addc_u32 s28, s4, 0
	s_movk_i32 s29, 0x4000
	s_movk_i32 s31, 0x2000
	s_mov_b64 s[8:9], 0
	s_mov_b32 s30, 0x41000000
	v_mov_b32_e32 v0, 0
	v_mov_b32_e32 v1, v188
	v_mov_b32_e32 v2, v188
	v_mov_b32_e32 v3, v188
	v_mov_b32_e32 v4, v188
	v_mov_b32_e32 v5, v188
	v_mov_b32_e32 v6, v188
	v_mov_b32_e32 v7, v188
	v_mov_b32_e32 v8, v188
	v_mov_b32_e32 v9, v188
	v_mov_b32_e32 v10, v188
	v_mov_b32_e32 v11, v188
	v_mov_b32_e32 v12, v188
	v_mov_b32_e32 v13, v188
	v_mov_b32_e32 v14, v188
	v_mov_b32_e32 v15, v188
	v_mov_b32_e32 v16, 0
	v_mov_b32_e32 v17, v188
	v_mov_b32_e32 v18, v188
	v_mov_b32_e32 v19, v188
	v_mov_b32_e32 v20, v188
	v_mov_b32_e32 v21, v188
	v_mov_b32_e32 v22, v188
	v_mov_b32_e32 v23, v188
	v_mov_b32_e32 v24, v188
	v_mov_b32_e32 v25, v188
	v_mov_b32_e32 v26, v188
	v_mov_b32_e32 v27, v188
	v_mov_b32_e32 v28, v188
	v_mov_b32_e32 v29, v188
	v_mov_b32_e32 v30, v188
	v_mov_b32_e32 v31, v188
	s_cmp_lt_u32 s20, 4
	s_cbranch_scc0 .Lattn_prio_done
	s_setprio 1
